# speedup vs baseline: 1.0251x; 1.0133x over previous
_Z6gat_k1PKfS0_S0_S0_PDF16_S1_S1_Pf:
	s_load_dwordx8 s[4:11], s[0:1], 0x0
	s_load_dwordx8 s[12:19], s[0:1], 0x20
	v_lshrrev_b32_e32 v54, 6, v0
	v_bfe_u32 v123, v0, 4, 2
	v_and_b32_e32 v120, 15, v0
	v_lshlrev_b32_e32 v120, 4, v120
	v_lshl_or_b32 v120, v54, 8, v120
	v_mov_b32_e32 v121, 0
	v_and_b32_e32 v57, 0xc0, v0
	s_lshl_b32 s3, s2, 5
	v_and_b32_e32 v1, 63, v0
	v_bfe_u32 v55, v0, 5, 1
	v_lshlrev_b32_e32 v2, 8, v57
	v_mov_b32_e32 v19, 0
	v_or_b32_e32 v4, s3, v123
	v_and_b32_e32 v56, 31, v0
	v_lshl_or_b32 v18, v55, 11, v2
	v_lshlrev_b32_e32 v20, 4, v1
	v_mov_b32_e32 v21, v19
	v_ashrrev_i32_e32 v5, 31, v4
	s_waitcnt lgkmcnt(0)
	v_lshl_add_u64 v[2:3], s[6:7], 0, v[18:19]
	v_lshlrev_b32_e32 v18, 2, v56
	v_lshl_add_u64 v[6:7], s[4:5], 0, v[120:121]
	s_movk_i32 s4, 0x410
	v_mad_u32_u24 v122, v123, s4, v120
	v_lshlrev_b64 v[8:9], 10, v[4:5]
	v_lshl_add_u64 v[2:3], v[2:3], 0, v[18:19]
	v_lshl_add_u64 v[10:11], v[6:7], 0, v[8:9]
	v_or_b32_e32 v12, 0x1000, v8
	v_mov_b32_e32 v13, v9
	global_load_dword v58, v[2:3], off
	global_load_dword v59, v[2:3], off offset:128
	global_load_dword v60, v[2:3], off offset:256
	global_load_dword v61, v[2:3], off offset:384
	global_load_dword v62, v[2:3], off offset:512
	global_load_dword v63, v[2:3], off offset:640
	global_load_dword v64, v[2:3], off offset:768
	global_load_dword v65, v[2:3], off offset:896
	v_lshl_add_u64 v[12:13], v[6:7], 0, v[12:13]
	global_load_dwordx4 v[22:25], v[10:11], off nt
	global_load_dwordx4 v[26:29], v[12:13], off nt
	v_or_b32_e32 v10, 0x2000, v8
	v_mov_b32_e32 v11, v9
	v_or_b32_e32 v8, 0x3000, v8
	v_lshl_add_u64 v[10:11], v[6:7], 0, v[10:11]
	v_lshl_add_u64 v[8:9], v[6:7], 0, v[8:9]
	global_load_dwordx4 v[30:33], v[10:11], off nt
	global_load_dwordx4 v[34:37], v[8:9], off nt
	v_or_b32_e32 v8, 16, v4
	v_ashrrev_i32_e32 v9, 31, v8
	v_or_b32_e32 v10, 20, v4
	v_lshlrev_b64 v[8:9], 10, v[8:9]
	v_ashrrev_i32_e32 v11, 31, v10
	v_lshl_add_u64 v[8:9], v[6:7], 0, v[8:9]
	v_lshlrev_b64 v[10:11], 10, v[10:11]
	v_lshl_add_u64 v[10:11], v[6:7], 0, v[10:11]
	global_load_dwordx4 v[38:41], v[8:9], off nt
	global_load_dwordx4 v[42:45], v[10:11], off nt
	v_or_b32_e32 v8, 24, v4
	v_ashrrev_i32_e32 v9, 31, v8
	v_or_b32_e32 v4, 28, v4
	v_lshlrev_b64 v[8:9], 10, v[8:9]
	v_ashrrev_i32_e32 v5, 31, v4
	v_lshl_add_u64 v[8:9], v[6:7], 0, v[8:9]
	v_lshlrev_b64 v[4:5], 10, v[4:5]
	v_lshl_add_u64 v[4:5], v[6:7], 0, v[4:5]
	global_load_dwordx4 v[46:49], v[8:9], off nt
	global_load_dwordx4 v[50:53], v[4:5], off nt
	global_load_dword v19, v[2:3], off offset:1024
	global_load_dword v66, v[2:3], off offset:1152
	global_load_dword v67, v[2:3], off offset:1280
	global_load_dword v68, v[2:3], off offset:1408
	global_load_dword v69, v[2:3], off offset:1536
	global_load_dword v70, v[2:3], off offset:1664
	global_load_dword v71, v[2:3], off offset:1792
	global_load_dword v72, v[2:3], off offset:1920
	s_movk_i32 s4, 0x1000
	v_add_co_u32_e32 v4, vcc, s4, v2
	s_movk_i32 s4, 0x2000
	s_nop 0
	v_addc_co_u32_e32 v5, vcc, 0, v3, vcc
	v_add_co_u32_e32 v6, vcc, s4, v2
	s_movk_i32 s4, 0x3000
	s_nop 0
	v_addc_co_u32_e32 v7, vcc, 0, v3, vcc
	global_load_dword v73, v[4:5], off offset:128
	global_load_dword v74, v[4:5], off offset:256
	global_load_dword v75, v[4:5], off offset:384
	global_load_dword v76, v[4:5], off offset:512
	global_load_dword v77, v[4:5], off offset:640
	global_load_dword v78, v[4:5], off offset:768
	global_load_dword v79, v[4:5], off offset:896
	global_load_dword v80, v[4:5], off offset:1024
	global_load_dword v81, v[4:5], off offset:1152
	global_load_dword v82, v[4:5], off offset:1280
	global_load_dword v83, v[4:5], off offset:1408
	global_load_dword v84, v[4:5], off offset:1536
	global_load_dword v85, v[4:5], off offset:1664
	global_load_dword v86, v[4:5], off offset:1792
	global_load_dword v87, v[4:5], off offset:1920
	global_load_dword v88, v[6:7], off offset:-4096
	global_load_dword v89, v[6:7], off
	global_load_dword v90, v[6:7], off offset:128
	global_load_dword v91, v[6:7], off offset:256
	global_load_dword v92, v[6:7], off offset:384
	global_load_dword v93, v[6:7], off offset:512
	global_load_dword v94, v[6:7], off offset:640
	global_load_dword v95, v[6:7], off offset:768
	global_load_dword v96, v[6:7], off offset:896
	global_load_dword v97, v[6:7], off offset:1024
	global_load_dword v98, v[6:7], off offset:1152
	global_load_dword v99, v[6:7], off offset:1280
	global_load_dword v100, v[6:7], off offset:1408
	global_load_dword v101, v[6:7], off offset:1536
	global_load_dword v102, v[6:7], off offset:1664
	global_load_dword v103, v[6:7], off offset:1792
	global_load_dword v104, v[6:7], off offset:1920
	v_add_co_u32_e32 v2, vcc, s4, v2
	v_and_b32_e32 v1, 7, v0
	s_nop 0
	v_addc_co_u32_e32 v3, vcc, 0, v3, vcc
	global_load_dword v105, v[2:3], off
	global_load_dword v106, v[2:3], off offset:128
	global_load_dword v107, v[2:3], off offset:256
	global_load_dword v108, v[2:3], off offset:384
	global_load_dword v109, v[2:3], off offset:512
	global_load_dword v110, v[2:3], off offset:640
	global_load_dword v111, v[2:3], off offset:768
	global_load_dword v112, v[2:3], off offset:896
	global_load_dword v113, v[2:3], off offset:1024
	global_load_dword v114, v[2:3], off offset:1152
	global_load_dword v115, v[2:3], off offset:1280
	global_load_dword v116, v[2:3], off offset:1408
	global_load_dword v117, v[2:3], off offset:1536
	global_load_dword v118, v[2:3], off offset:1664
	global_load_dword v119, v[2:3], off offset:1792
	global_load_dword v120, v[2:3], off offset:1920
	v_lshlrev_b32_e32 v121, 5, v1
	global_load_dwordx4 v[6:9], v121, s[8:9]
	global_load_dwordx4 v[2:5], v121, s[10:11]
	global_load_dwordx4 v[14:17], v121, s[8:9] offset:16
	global_load_dwordx4 v[10:13], v121, s[10:11] offset:16
	s_movk_i32 s8, 0x110
	s_waitcnt vmcnt(62)
	ds_write_b128 v122, v[22:25] offset:34816
	ds_write_b128 v122, v[26:29] offset:38976
	ds_write_b128 v122, v[30:33] offset:43136
	ds_write_b128 v122, v[34:37] offset:47296
	ds_write_b128 v122, v[38:41] offset:51456
	ds_write_b128 v122, v[42:45] offset:55616
	s_waitcnt vmcnt(61)
	ds_write_b128 v122, v[46:49] offset:59776
	s_waitcnt vmcnt(60)
	ds_write_b128 v122, v[50:53] offset:63936
	v_mul_u32_u24_e32 v22, 0x410, v56
	v_lshlrev_b32_e32 v23, 2, v57
	v_and_b32_e32 v24, 32, v0
	v_add3_u32 v38, v22, v23, v24
	s_waitcnt lgkmcnt(0)
	ds_read_b128 v[22:25], v38 offset:34832
	ds_read_b128 v[26:29], v38 offset:34816
	ds_read_b128 v[30:33], v38 offset:34880
	ds_read_b128 v[34:37], v38 offset:34896
	s_waitcnt lgkmcnt(3)
	v_cvt_pk_f16_f32 v25, v24, v25
	v_cvt_pk_f16_f32 v24, v22, v23
	s_waitcnt lgkmcnt(2)
	v_cvt_pk_f16_f32 v23, v28, v29
	v_cvt_pk_f16_f32 v22, v26, v27
	s_waitcnt vmcnt(53)
	v_cvt_pk_f16_f32 v29, v69, v71
	v_cvt_pk_f16_f32 v28, v19, v67
	v_cvt_pk_f16_f32 v27, v62, v64
	v_cvt_pk_f16_f32 v26, v58, v60
	v_lshlrev_b32_e32 v19, 2, v55
	s_nop 0
	v_mfma_f32_32x32x16_f16 a[0:15], v[22:25], v[26:29], 0
	s_waitcnt vmcnt(52)
	v_cvt_pk_f16_f32 v29, v70, v72
	v_cvt_pk_f16_f32 v28, v66, v68
	v_cvt_pk_f16_f32 v27, v63, v65
	v_cvt_pk_f16_f32 v26, v59, v61
	s_nop 1
	v_mfma_f32_32x32x16_f16 a[16:31], v[22:25], v[26:29], 0
	s_waitcnt lgkmcnt(0)
	v_cvt_pk_f16_f32 v25, v36, v37
	v_cvt_pk_f16_f32 v24, v34, v35
	v_cvt_pk_f16_f32 v23, v32, v33
	v_cvt_pk_f16_f32 v22, v30, v31
	ds_read_b128 v[30:33], v38 offset:34944
	ds_read_b128 v[34:37], v38 offset:34960
	s_waitcnt vmcnt(38)
	v_cvt_pk_f16_f32 v29, v84, v86
	v_cvt_pk_f16_f32 v28, v80, v82
	v_cvt_pk_f16_f32 v27, v76, v78
	s_waitcnt vmcnt(36)
	v_cvt_pk_f16_f32 v26, v88, v74
	s_nop 1
	v_mfma_f32_32x32x16_f16 a[0:15], v[22:25], v[26:29], a[0:15]
	v_cvt_pk_f16_f32 v29, v85, v87
	v_cvt_pk_f16_f32 v28, v81, v83
	v_cvt_pk_f16_f32 v27, v77, v79
	v_cvt_pk_f16_f32 v26, v73, v75
	s_nop 1
	v_mfma_f32_32x32x16_f16 a[16:31], v[22:25], v[26:29], a[16:31]
	s_waitcnt lgkmcnt(0)
	v_cvt_pk_f16_f32 v25, v36, v37
	v_cvt_pk_f16_f32 v24, v34, v35
	v_cvt_pk_f16_f32 v23, v32, v33
	v_cvt_pk_f16_f32 v22, v30, v31
	ds_read_b128 v[30:33], v38 offset:35008
	ds_read_b128 v[34:37], v38 offset:35024
	s_waitcnt vmcnt(21)
	v_cvt_pk_f16_f32 v29, v101, v103
	v_cvt_pk_f16_f32 v28, v97, v99
	v_cvt_pk_f16_f32 v27, v93, v95
	v_cvt_pk_f16_f32 v26, v89, v91
	s_nop 1
	v_mfma_f32_32x32x16_f16 a[0:15], v[22:25], v[26:29], a[0:15]
	s_waitcnt vmcnt(20)
	v_cvt_pk_f16_f32 v29, v102, v104
	v_cvt_pk_f16_f32 v28, v98, v100
	v_cvt_pk_f16_f32 v27, v94, v96
	v_cvt_pk_f16_f32 v26, v90, v92
	s_nop 1
	v_mfma_f32_32x32x16_f16 a[16:31], v[22:25], v[26:29], a[16:31]
	s_waitcnt lgkmcnt(0)
	v_cvt_pk_f16_f32 v25, v36, v37
	v_cvt_pk_f16_f32 v24, v34, v35
	v_cvt_pk_f16_f32 v23, v32, v33
	v_cvt_pk_f16_f32 v22, v30, v31
	s_waitcnt vmcnt(5)
	v_cvt_pk_f16_f32 v29, v117, v119
	v_cvt_pk_f16_f32 v28, v113, v115
	v_cvt_pk_f16_f32 v27, v109, v111
	v_cvt_pk_f16_f32 v26, v105, v107
	s_nop 1
	v_mfma_f32_32x32x16_f16 a[0:15], v[22:25], v[26:29], a[0:15]
	s_waitcnt vmcnt(4)
	v_cvt_pk_f16_f32 v29, v118, v120
	v_cvt_pk_f16_f32 v28, v114, v116
	v_cvt_pk_f16_f32 v27, v110, v112
	v_cvt_pk_f16_f32 v26, v106, v108
	s_nop 1
	v_mfma_f32_32x32x16_f16 a[16:31], v[22:25], v[26:29], a[16:31]
	v_lshl_or_b32 v22, v54, 5, v19
	v_mul_u32_u24_e32 v22, 0x44, v22
	v_lshl_add_u32 v22, v22, 2, v18
	s_nop 0
	ds_write_b32 v22, a0
	s_nop 6
	ds_write_b32 v22, a16 offset:128
	ds_write_b32 v22, a1 offset:272
	ds_write_b32 v22, a17 offset:400
	ds_write_b32 v22, a2 offset:544
	ds_write_b32 v22, a18 offset:672
	ds_write_b32 v22, a3 offset:816
	ds_write_b32 v22, a19 offset:944
	ds_write_b32 v22, a4 offset:2176
	ds_write_b32 v22, a20 offset:2304
	ds_write_b32 v22, a5 offset:2448
	ds_write_b32 v22, a21 offset:2576
	ds_write_b32 v22, a6 offset:2720
	ds_write_b32 v22, a22 offset:2848
	ds_write_b32 v22, a7 offset:2992
	ds_write_b32 v22, a23 offset:3120
	ds_write_b32 v22, a8 offset:4352
	ds_write_b32 v22, a24 offset:4480
	ds_write_b32 v22, a9 offset:4624
	ds_write_b32 v22, a25 offset:4752
	ds_write_b32 v22, a10 offset:4896
	ds_write_b32 v22, a26 offset:5024
	ds_write_b32 v22, a11 offset:5168
	ds_write_b32 v22, a27 offset:5296
	ds_write_b32 v22, a12 offset:6528
	ds_write_b32 v22, a28 offset:6656
	ds_write_b32 v22, a13 offset:6800
	ds_write_b32 v22, a29 offset:6928
	ds_write_b32 v22, a14 offset:7072
	ds_write_b32 v22, a30 offset:7200
	ds_write_b32 v22, a15 offset:7344
	ds_write_b32 v22, a31 offset:7472
	v_lshrrev_b32_e32 v22, 3, v0
	v_mad_u32_u24 v23, v22, s8, v121
	s_waitcnt lgkmcnt(0)
	s_barrier
	ds_read_b128 v[24:27], v23
	ds_read_b128 v[28:31], v23 offset:16
	ds_read_b128 v[32:35], v23 offset:8704
	s_waitcnt lgkmcnt(2)
	v_pk_add_f32 v[36:37], v[26:27], 0 op_sel_hi:[1,0]
	v_pk_add_f32 v[38:39], v[24:25], 0 op_sel_hi:[1,0]
	ds_read_b128 v[24:27], v23 offset:8720
	s_waitcnt lgkmcnt(2)
	v_pk_add_f32 v[40:41], v[30:31], 0 op_sel_hi:[1,0]
	v_pk_add_f32 v[42:43], v[28:29], 0 op_sel_hi:[1,0]
	ds_read_b128 v[28:31], v23 offset:17408
	s_waitcnt lgkmcnt(2)
	v_pk_add_f32 v[34:35], v[36:37], v[34:35]
	v_pk_add_f32 v[36:37], v[38:39], v[32:33]
	s_waitcnt lgkmcnt(1)
	v_pk_add_f32 v[38:39], v[40:41], v[26:27]
	v_pk_add_f32 v[40:41], v[42:43], v[24:25]
	ds_read_b128 v[24:27], v23 offset:17424
	s_waitcnt lgkmcnt(1)
	v_pk_add_f32 v[42:43], v[34:35], v[30:31]
	ds_read_b128 v[30:33], v23 offset:26112
	v_pk_add_f32 v[28:29], v[36:37], v[28:29]
	ds_read_b128 v[34:37], v23 offset:26128
	s_waitcnt lgkmcnt(2)
	v_pk_add_f32 v[40:41], v[40:41], v[24:25]
	v_pk_add_f32 v[38:39], v[38:39], v[26:27]
	s_waitcnt lgkmcnt(1)
	v_pk_add_f32 v[24:25], v[28:29], v[30:31]
	v_pk_add_f32 v[26:27], v[42:43], v[32:33]
	s_waitcnt lgkmcnt(0)
	v_pk_add_f32 v[28:29], v[40:41], v[34:35]
	v_pk_add_f32 v[30:31], v[38:39], v[36:37]
	s_waitcnt vmcnt(0)
	v_mul_f32_e32 v10, v28, v10
	v_fmac_f32_e32 v10, v24, v2
	v_mul_f32_e32 v14, v28, v14
	v_add_f32_e32 v2, 0, v10
	v_mul_f32_e32 v10, v29, v15
	v_fmac_f32_e32 v14, v24, v6
	v_fmac_f32_e32 v10, v25, v7
	v_mul_f32_e32 v7, v29, v11
	v_add_f32_e32 v6, 0, v14
	v_fmac_f32_e32 v7, v25, v3
	v_mul_f32_e32 v3, v30, v16
	v_add_f32_e32 v6, v6, v10
	v_fmac_f32_e32 v3, v26, v8
	v_add_f32_e32 v3, v6, v3
	v_mul_f32_e32 v6, v30, v12
	v_fmac_f32_e32 v6, v26, v4
	v_mul_f32_e32 v4, v31, v17
	v_fmac_f32_e32 v4, v27, v9
	v_add_f32_e32 v2, v2, v7
	v_add_f32_e32 v3, v3, v4
	v_mul_f32_e32 v4, v31, v13
	v_add_f32_e32 v2, v2, v6
	v_fmac_f32_e32 v4, v27, v5
	v_add_f32_e32 v2, v2, v4
	ds_write_b128 v23, v[24:27]
	ds_write_b128 v23, v[28:31] offset:16
	s_nop 1
	v_add_f32_dpp v3, v3, v3 quad_perm:[1,0,3,2] row_mask:0xf bank_mask:0xf
	v_add_f32_dpp v6, v2, v2 quad_perm:[1,0,3,2] row_mask:0xf bank_mask:0xf
	s_nop 1
	v_add_f32_dpp v3, v3, v3 quad_perm:[2,3,0,1] row_mask:0xf bank_mask:0xf
	v_add_f32_dpp v6, v6, v6 quad_perm:[2,3,0,1] row_mask:0xf bank_mask:0xf
	s_nop 1
	v_add_f32_dpp v2, v3, v3 row_half_mirror row_mask:0xf bank_mask:0xf
	v_add_f32_dpp v3, v6, v6 row_half_mirror row_mask:0xf bank_mask:0xf
	v_cmp_eq_u32_e32 vcc, 0, v1
	s_and_saveexec_b64 s[6:7], vcc
	s_cbranch_execz .LBB0_2
	v_mul_f32_e32 v4, 0x3f7d70a4, v3
	v_mul_f32_e32 v4, 0x3fb8aa3b, v4
	v_mul_f32_e32 v3, 0x3c23d70a, v3
	v_exp_f32_e32 v4, v4
	v_mul_f32_e32 v3, 0x3fb8aa3b, v3
	v_exp_f32_e32 v3, v3
	v_lshlrev_b32_e32 v5, 2, v22
	v_or_b32_e32 v6, 0x10a80, v5
	v_mul_f32_e32 v2, 0xbf7d70a4, v2
	ds_write_b32 v6, v4
	v_or_b32_e32 v4, 0x10a00, v5
	v_mul_f32_e32 v2, 0x3fb8aa3b, v2
	ds_write_b32 v4, v3
	v_exp_f32_e32 v4, v2
	v_add_u32_e32 v2, s3, v22
	v_ashrrev_i32_e32 v3, 31, v2
	v_lshl_add_u64 v[2:3], v[2:3], 2, s[18:19]
	global_store_dword v[2:3], v4, off sc1
